# v43 with the priority raise of waves 4-7 limited to their first two mask rows
# baseline (speedup 1.0000x reference)
_Z7k_gemm1PKfS0_PKDv4_jPKiPiS6_P15HIP_vector_typeIiLj2EEPDF16_S0_S6_S9_:
	v_lshrrev_b32_e32 v142, 6, v0
	s_mov_b32 s10, s2
	v_readfirstlane_b32 s90, v0
	s_nop 0
	s_mov_b32 s91, 0
	s_cmp_lt_u32 s90, 0x100
	s_cbranch_scc1 .Lg1_prio_done
	s_cmp_ge_u32 s90, 0x200
	s_cbranch_scc1 .Lg1_prio_done
	s_setprio 1

.LBB1_3:
	s_or_b64 exec, exec, s[2:3]
	s_add_u32 s91, s91, 1
	s_cmp_lt_u32 s91, 2
	s_cbranch_scc1 .Lg1_keep_prio
	s_setprio 0
.Lg1_keep_prio:
	v_add_u32_e32 v2, 12, v142
	v_cmp_lt_u32_e32 vcc, 19, v142
	s_or_b64 s[34:35], vcc, s[34:35]
	v_mov_b32_e32 v142, v2
	s_andn2_b64 exec, exec, s[34:35]
	s_cbranch_execz .LBB1_232
